# baseline (speedup 1.0000x reference)
_Z4khidPKDF16_PKfS2_S2_S0_PDF16_Pf:
	s_load_dwordx8 s[4:11], s[0:1], 0x0
	s_load_dwordx2 s[12:13], s[0:1], 0x20
	s_load_dwordx2 s[22:23], s[0:1], 0x30
	v_lshlrev_b32_e32 v1, 3, v0
	s_lshr_b32 s3, s2, 1
	v_and_b32_e32 v2, 56, v1
	s_and_b32 s15, s3, 0x7ffffffc
	s_lshl_b32 s14, s2, 4
	v_lshlrev_b32_e32 v106, 1, v2
	v_mov_b32_e32 v107, 0
	s_and_b32 s14, s14, 0x70
	v_lshlrev_b32_e32 v126, 2, v2
	s_add_i32 s16, s15, -1
	s_waitcnt lgkmcnt(0)
	v_and_b32_e32 v132, 63, v0
	v_lshlrev_b32_e32 v132, 3, v132
	global_load_dwordx2 v[108:109], v132, s[6:7]
	global_load_dwordx2 v[134:135], v132, s[6:7] offset:512
	global_load_dwordx2 v[136:137], v132, s[6:7] offset:1024
	global_load_dwordx2 v[138:139], v132, s[6:7] offset:1536
	v_lshl_add_u64 v[2:3], s[4:5], 0, v[106:107]
	v_mul_u32_u24_e32 v1, 0x1c8, v0
	s_movk_i32 s4, 0xffee
	v_lshrrev_b32_e32 v114, 3, v0
	s_add_i32 s17, s14, -1
	v_mul_i32_i24_sdwa v4, v1, s4 dst_sel:DWORD dst_unused:UNUSED_PAD src0_sel:WORD_1 src1_sel:DWORD
	v_add_u32_sdwa v124, s16, v1 dst_sel:DWORD dst_unused:UNUSED_PAD src0_sel:DWORD src1_sel:WORD_1
	s_movk_i32 s4, 0x7f
	v_add3_u32 v125, s17, v114, v4
	v_med3_i32 v1, v124, 0, s4
	v_med3_i32 v4, v125, 0, s4
	v_lshlrev_b32_e32 v1, 14, v1
	v_or_b32_e32 v121, 32, v114
	v_lshl_or_b32 v106, v4, 7, v1
	v_mul_lo_u16_e32 v1, 57, v121
	v_lshrrev_b16_e32 v1, 10, v1
	v_mul_i32_i24_e32 v6, 0xffffffee, v1
	v_add_u32_e32 v122, s16, v1
	v_add3_u32 v123, s17, v121, v6
	v_min_u32_e32 v1, 0x7f, v122
	v_med3_i32 v6, v123, 0, s4
	v_lshlrev_b32_e32 v1, 14, v1
	v_or_b32_e32 v118, 64, v114
	v_lshl_add_u64 v[4:5], v[2:3], 0, v[106:107]
	v_lshl_or_b32 v106, v6, 7, v1
	v_mul_lo_u16_e32 v1, 57, v118
	v_lshrrev_b16_e32 v1, 10, v1
	v_lshl_add_u64 v[6:7], v[2:3], 0, v[106:107]
	global_load_dwordx4 v[86:89], v[4:5], off
	global_load_dwordx4 v[82:85], v[6:7], off
	v_mul_i32_i24_e32 v4, 0xffffffee, v1
	v_add_u32_e32 v119, s16, v1
	v_add3_u32 v120, s17, v118, v4
	v_min_u32_e32 v1, 0x7f, v119
	v_med3_i32 v4, v120, 0, s4
	v_lshlrev_b32_e32 v1, 14, v1
	v_or_b32_e32 v115, 0x60, v114
	v_lshl_or_b32 v106, v4, 7, v1
	v_mul_lo_u16_e32 v1, 57, v115
	v_lshrrev_b16_e32 v1, 10, v1
	v_mul_i32_i24_e32 v6, 0xffffffee, v1
	v_add_u32_e32 v116, s16, v1
	v_add3_u32 v117, s17, v115, v6
	v_min_u32_e32 v1, 0x7f, v116
	v_med3_i32 v6, v117, 0, s4
	v_lshlrev_b32_e32 v1, 14, v1
	v_lshrrev_b32_e32 v112, 6, v0
	v_lshl_add_u64 v[4:5], v[2:3], 0, v[106:107]
	v_lshl_or_b32 v106, v6, 7, v1
	v_mul_u32_u24_e32 v1, 0x480, v112
	v_and_b32_e32 v113, 63, v0
	v_lshl_add_u64 v[2:3], v[2:3], 0, v[106:107]
	v_lshlrev_b32_e32 v106, 4, v1
	global_load_dwordx4 v[78:81], v[4:5], off
	global_load_dwordx4 v[74:77], v[2:3], off
	v_lshl_add_u64 v[2:3], s[12:13], 0, v[106:107]
	v_lshlrev_b32_e32 v106, 4, v113
	v_lshl_add_u64 v[2:3], v[2:3], 0, v[106:107]
	s_movk_i32 s4, 0x1000
	v_add_co_u32_e32 v4, vcc, s4, v2
	s_movk_i32 s4, 0x2000
	s_nop 0
	v_addc_co_u32_e32 v5, vcc, 0, v3, vcc
	v_add_co_u32_e32 v90, vcc, s4, v2
	s_movk_i32 s4, 0x3000
	s_nop 0
	v_addc_co_u32_e32 v91, vcc, 0, v3, vcc
	v_add_co_u32_e32 v92, vcc, s4, v2
	s_movk_i32 s4, 0x4000
	s_nop 0
	v_addc_co_u32_e32 v93, vcc, 0, v3, vcc
	v_add_co_u32_e32 v110, vcc, s4, v2
	global_load_dwordx4 v[70:73], v[2:3], off
	global_load_dwordx4 v[66:69], v[2:3], off offset:1024
	v_addc_co_u32_e32 v111, vcc, 0, v3, vcc
	global_load_dwordx4 v[62:65], v[2:3], off offset:2048
	global_load_dwordx4 v[58:61], v[2:3], off offset:3072
	global_load_dwordx4 v[50:53], v[4:5], off offset:1024
	global_load_dwordx4 v[46:49], v[4:5], off offset:2048
	global_load_dwordx4 v[42:45], v[4:5], off offset:3072
	global_load_dwordx4 v[18:21], v[92:93], off offset:1024
	global_load_dwordx4 v[14:17], v[92:93], off offset:2048
	global_load_dwordx4 v[10:13], v[92:93], off offset:3072
	global_load_dwordx4 v[54:57], v[90:91], off offset:-4096
	global_load_dwordx4 v[38:41], v[90:91], off
	global_load_dwordx4 v[34:37], v[90:91], off offset:1024
	global_load_dwordx4 v[30:33], v[90:91], off offset:2048
	global_load_dwordx4 v[26:29], v[90:91], off offset:3072
	global_load_dwordx4 v[22:25], v[110:111], off offset:-4096
	global_load_dwordx4 v[6:9], v[110:111], off
	s_nop 0
	global_load_dwordx4 v[2:5], v[110:111], off offset:1024
	global_load_dwordx4 v[94:97], v126, s[8:9] offset:16
	global_load_dwordx4 v[90:93], v126, s[10:11] offset:16
	global_load_dwordx4 v[102:105], v126, s[8:9]
	global_load_dwordx4 v[98:101], v126, s[10:11]
	v_cmp_eq_u32_e64 s[4:5], 63, v113
	s_waitcnt vmcnt(26)
	v_pk_add_f32 v[108:109], v[108:109], v[134:135]
	v_pk_add_f32 v[136:137], v[136:137], v[138:139]
	v_pk_add_f32 v[108:109], v[108:109], v[136:137]
	s_nop 1
	v_mov_b32_dpp v110, v108 row_shr:1 row_mask:0xf bank_mask:0xf bound_ctrl:1
	v_mov_b32_dpp v111, v109 row_shr:1 row_mask:0xf bank_mask:0xf bound_ctrl:1
	v_pk_add_f32 v[108:109], v[108:109], v[110:111]
	v_lshlrev_b32_e32 v1, 3, v112
	s_nop 0
	v_mov_b32_dpp v110, v108 row_shr:2 row_mask:0xf bank_mask:0xf bound_ctrl:1
	v_mov_b32_dpp v111, v109 row_shr:2 row_mask:0xf bank_mask:0xf bound_ctrl:1
	v_pk_add_f32 v[108:109], v[108:109], v[110:111]
	s_nop 1
	v_mov_b32_dpp v110, v108 row_shr:4 row_mask:0xf bank_mask:0xf bound_ctrl:1
	v_mov_b32_dpp v111, v109 row_shr:4 row_mask:0xf bank_mask:0xf bound_ctrl:1
	v_pk_add_f32 v[108:109], v[108:109], v[110:111]
	s_nop 1
	v_mov_b32_dpp v110, v108 row_shr:8 row_mask:0xf bank_mask:0xf bound_ctrl:1
	v_mov_b32_dpp v111, v109 row_shr:8 row_mask:0xf bank_mask:0xf bound_ctrl:1
	v_pk_add_f32 v[108:109], v[108:109], v[110:111]
	v_mov_b32_e32 v110, v107
	v_mov_b32_e32 v111, v107
	s_nop 0
	v_mov_b32_dpp v110, v108 row_bcast:15 row_mask:0xa bank_mask:0xf
	v_mov_b32_dpp v111, v109 row_bcast:15 row_mask:0xa bank_mask:0xf
	v_pk_add_f32 v[108:109], v[108:109], v[110:111]
	v_mov_b32_e32 v110, 0
	v_mov_b32_e32 v111, 0
	s_nop 0
	v_mov_b32_dpp v110, v108 row_bcast:31 row_mask:0xc bank_mask:0xf
	v_mov_b32_dpp v111, v109 row_bcast:31 row_mask:0xc bank_mask:0xf
	v_pk_add_f32 v[108:109], v[108:109], v[110:111]
	s_mov_b32 s6, 0xf800000
	s_nop 0
	v_readlane_b32 s18, v108, 63
	v_readlane_b32 s19, v109, 63
	s_nop 3
	v_mov_b32_e32 v106, s18
	v_mov_b32_e32 v107, s19
	v_mul_f32_e32 v109, 0x35800000, v106
	v_mul_f32_e32 v106, 0x35800000, v107
	v_fma_f32 v106, -v109, v109, v106
	v_add_f32_e32 v106, 0x3727c5ac, v106
	v_mul_f32_e32 v107, 0x4f800000, v106
	v_cmp_gt_f32_e32 vcc, s6, v106
	s_nop 1
	v_cndmask_b32_e32 v106, v106, v107, vcc
	v_sqrt_f32_e32 v107, v106
	s_nop 0
	v_add_u32_e32 v108, -1, v107
	v_fma_f32 v110, -v108, v107, v106
	v_cmp_ge_f32_e64 s[6:7], 0, v110
	v_add_u32_e32 v110, 1, v107
	s_nop 0
	v_cndmask_b32_e64 v108, v107, v108, s[6:7]
	v_fma_f32 v107, -v110, v107, v106
	v_cmp_lt_f32_e64 s[6:7], 0, v107
	s_nop 1
	v_cndmask_b32_e64 v107, v108, v110, s[6:7]
	v_mul_f32_e32 v108, 0x37800000, v107
	v_cndmask_b32_e32 v107, v107, v108, vcc
	v_mov_b32_e32 v108, 0x260
	v_cmp_class_f32_e32 vcc, v106, v108
	s_nop 1
	v_cndmask_b32_e32 v106, v107, v106, vcc
	v_div_scale_f32 v107, s[6:7], v106, v106, 1.0
	v_rcp_f32_e32 v108, v107
	s_movk_i32 s6, 0x360
	v_cmp_gt_u32_e64 s[6:7], s6, v0
	v_fma_f32 v110, -v107, v108, 1.0
	v_fmac_f32_e32 v108, v110, v108
	v_div_scale_f32 v110, vcc, 1.0, v106, 1.0
	v_mul_f32_e32 v111, v110, v108
	v_fma_f32 v126, -v107, v111, v110
	v_fmac_f32_e32 v111, v126, v108
	v_fma_f32 v107, -v107, v111, v110
	v_div_fmas_f32 v107, v107, v108, v111
	v_div_fixup_f32 v110, v107, v106, 1.0
	s_waitcnt vmcnt(1)
	v_mul_f32_e32 v102, v110, v102
	v_mul_f32_e32 v94, v110, v94
	s_waitcnt vmcnt(0)
	v_fma_f32 v106, -v109, v102, v98
	v_fma_f32 v98, -v109, v94, v90
	v_mul_f32_e32 v107, v110, v103
	v_mul_f32_e32 v95, v110, v95
	v_xor_b32_e32 v90, v114, v0
	v_fma_f32 v108, -v109, v107, v99
	v_fma_f32 v99, -v109, v95, v91
	v_mul_f32_e32 v103, v110, v104
	v_mul_f32_e32 v91, v110, v96
	v_mul_f32_e32 v104, v110, v105
	v_mul_f32_e32 v96, v110, v97
	v_lshlrev_b32_e32 v90, 4, v90
	v_fma_f32 v100, -v109, v103, v100
	v_fma_f32 v92, -v109, v91, v92
	v_fma_f32 v97, -v109, v104, v101
	v_fma_f32 v93, -v109, v96, v93
	v_and_b32_e32 v90, 0x70, v90
	v_fma_mixlo_f16 v101, v86, v102, v106 op_sel_hi:[1,0,0]
	v_fma_mixhi_f16 v101, v86, v107, v108 op_sel:[1,0,0] op_sel_hi:[1,0,0]
	v_pk_max_f16 v101, v101, 0
	v_fma_mixlo_f16 v86, v87, v103, v100 op_sel_hi:[1,0,0]
	v_fma_mixhi_f16 v86, v87, v104, v97 op_sel:[1,0,0] op_sel_hi:[1,0,0]
	v_pk_max_f16 v86, v86, 0
	v_fma_mixlo_f16 v87, v88, v94, v98 op_sel_hi:[1,0,0]
	v_fma_mixhi_f16 v87, v88, v95, v99 op_sel:[1,0,0] op_sel_hi:[1,0,0]
	v_pk_max_f16 v87, v87, 0
	v_fma_mixlo_f16 v88, v89, v91, v92 op_sel_hi:[1,0,0]
	v_fma_mixhi_f16 v88, v89, v96, v93 op_sel:[1,0,0] op_sel_hi:[1,0,0]
	v_pk_max_f16 v88, v88, 0
	s_and_saveexec_b64 s[8:9], s[6:7]
	s_cbranch_execz .LBB1_4
	v_or_b32_e32 v89, v125, v124
	s_movk_i32 s6, 0x80
	v_cmp_gt_u32_e32 vcc, s6, v89
	v_lshl_or_b32 v105, v114, 7, v90
	s_nop 0
	v_cndmask_b32_e32 v89, 0, v88, vcc
	v_cndmask_b32_e32 v88, 0, v87, vcc
	v_cndmask_b32_e32 v87, 0, v86, vcc
	v_cndmask_b32_e32 v86, 0, v101, vcc
	ds_write_b128 v105, v[86:89]

.LBB1_10:
	s_or_b64 exec, exec, s[8:9]
	v_lshrrev_b32_e32 v75, 4, v113
	v_and_b32_e32 v74, 15, v0
	v_lshlrev_b32_e32 v92, 7, v74
	v_bitop3_b32 v76, v0, v75, 7 bitop3:0x6c
	v_lshl_or_b32 v108, v76, 4, v92
	s_waitcnt lgkmcnt(0)
	s_barrier
	ds_read_b128 v[76:79], v108
	v_add_u32_e32 v96, 18, v74
	v_add_u32_e32 v100, 36, v74
	v_lshlrev_b32_e32 v97, 7, v96
	v_bitop3_b32 v80, v96, v75, 7 bitop3:0x6c
	v_lshlrev_b32_e32 v101, 7, v100
	v_bitop3_b32 v84, v100, v75, 7 bitop3:0x6c
	v_lshl_or_b32 v109, v80, 4, v97
	v_lshl_or_b32 v110, v84, 4, v101
	v_add_u32_e32 v104, 54, v74
	v_or_b32_e32 v113, 4, v75
	v_add_u32_e32 v118, 1, v74
	ds_read_b128 v[80:83], v109
	ds_read_b128 v[84:87], v110
	v_lshlrev_b32_e32 v105, 7, v104
	v_bitop3_b32 v88, v104, v75, 7 bitop3:0x6c
	v_bitop3_b32 v93, v0, v113, 7 bitop3:0x6c
	v_bitop3_b32 v96, v96, v113, 7 bitop3:0x6c
	v_bitop3_b32 v100, v100, v113, 7 bitop3:0x6c
	v_bitop3_b32 v104, v104, v113, 7 bitop3:0x6c
	v_lshlrev_b32_e32 v119, 7, v118
	v_bitop3_b32 v120, v118, v75, 7 bitop3:0x6c
	v_lshl_or_b32 v111, v88, 4, v105
	v_lshl_or_b32 v114, v93, 4, v92
	v_lshl_or_b32 v115, v96, 4, v97
	v_lshl_or_b32 v116, v100, 4, v101
	v_lshl_or_b32 v117, v104, 4, v105
	v_lshl_or_b32 v120, v120, 4, v119
	ds_read_b128 v[88:91], v111
	ds_read_b128 v[92:95], v114
	ds_read_b128 v[96:99], v115
	ds_read_b128 v[100:103], v116
	ds_read_b128 v[104:107], v117
	s_waitcnt lgkmcnt(7)
	v_mfma_f32_16x16x32_f16 a[0:3], v[70:73], v[76:79], 0
	ds_read_b128 v[76:79], v120
	v_add_u32_e32 v120, 19, v74
	v_lshlrev_b32_e32 v121, 7, v120
	v_bitop3_b32 v122, v120, v75, 7 bitop3:0x6c
	v_lshl_or_b32 v122, v122, 4, v121
	v_add_u32_e32 v123, 37, v74
	v_add_u32_e32 v126, 55, v74
	s_waitcnt lgkmcnt(7)
	v_mfma_f32_16x16x32_f16 a[4:7], v[70:73], v[80:83], 0
	ds_read_b128 v[80:83], v122
	v_lshlrev_b32_e32 v124, 7, v123
	v_bitop3_b32 v125, v123, v75, 7 bitop3:0x6c
	s_waitcnt lgkmcnt(7)
	v_mfma_f32_16x16x32_f16 a[8:11], v[70:73], v[84:87], 0
	v_lshlrev_b32_e32 v127, 7, v126
	v_bitop3_b32 v128, v126, v75, 7 bitop3:0x6c
	v_lshl_or_b32 v125, v125, 4, v124
	v_lshl_or_b32 v128, v128, 4, v127
	ds_read_b128 v[84:87], v125
	s_waitcnt lgkmcnt(7)
	v_mfma_f32_16x16x32_f16 a[12:15], v[70:73], v[88:91], 0
	ds_read_b128 v[70:73], v128
	v_bitop3_b32 v88, v118, v113, 7 bitop3:0x6c
	v_lshl_or_b32 v88, v88, 4, v119
	s_waitcnt lgkmcnt(7)
	v_mfma_f32_16x16x32_f16 a[0:3], v[66:69], v[92:95], a[0:3]
	v_bitop3_b32 v92, v120, v113, 7 bitop3:0x6c
	v_lshl_or_b32 v118, v92, 4, v121
	ds_read_b128 v[88:91], v88
	s_waitcnt lgkmcnt(7)
	v_mfma_f32_16x16x32_f16 a[4:7], v[66:69], v[96:99], a[4:7]
	ds_read_b128 v[92:95], v118
	v_bitop3_b32 v96, v123, v113, 7 bitop3:0x6c
	v_lshl_or_b32 v119, v96, 4, v124
	s_waitcnt lgkmcnt(7)
	v_mfma_f32_16x16x32_f16 a[8:11], v[66:69], v[100:103], a[8:11]
	v_add_u32_e32 v101, 2, v74
	v_bitop3_b32 v100, v126, v113, 7 bitop3:0x6c
	v_lshlrev_b32_e32 v102, 7, v101
	v_bitop3_b32 v103, v101, v75, 7 bitop3:0x6c
	v_lshl_or_b32 v100, v100, 4, v127
	v_lshl_or_b32 v103, v103, 4, v102
	ds_read_b128 v[96:99], v119
	s_waitcnt lgkmcnt(7)
	v_mfma_f32_16x16x32_f16 a[12:15], v[66:69], v[104:107], a[12:15]
	ds_read_b128 v[66:69], v100
	v_add_u32_e32 v106, 38, v74
	v_lshlrev_b32_e32 v107, 7, v106
	s_waitcnt lgkmcnt(7)
	v_mfma_f32_16x16x32_f16 a[0:3], v[62:65], v[76:79], a[0:3]
	ds_read_b128 v[76:79], v103
	v_add_u32_e32 v103, 20, v74
	v_lshlrev_b32_e32 v104, 7, v103
	v_bitop3_b32 v105, v103, v75, 7 bitop3:0x6c
	v_lshl_or_b32 v105, v105, 4, v104
	s_waitcnt lgkmcnt(7)
	v_mfma_f32_16x16x32_f16 a[4:7], v[62:65], v[80:83], a[4:7]
	ds_read_b128 v[80:83], v105
	s_lshl_b32 s3, s3, 7
	s_or_b32 s3, s3, 0x180
	s_waitcnt lgkmcnt(7)
	v_mfma_f32_16x16x32_f16 a[8:11], v[62:65], v[84:87], a[8:11]
	v_bitop3_b32 v84, v106, v75, 7 bitop3:0x6c
	v_lshl_or_b32 v120, v84, 4, v107
	ds_read_b128 v[84:87], v120
	s_waitcnt lgkmcnt(7)
	v_mfma_f32_16x16x32_f16 a[12:15], v[62:65], v[70:73], a[12:15]
	v_bitop3_b32 v70, v101, v113, 7 bitop3:0x6c
	ds_read_b128 v[62:65], v108 offset:7168
	v_lshl_or_b32 v70, v70, 4, v102
	s_waitcnt lgkmcnt(7)
	v_mfma_f32_16x16x32_f16 a[0:3], v[58:61], v[88:91], a[0:3]
	v_bitop3_b32 v88, v103, v113, 7 bitop3:0x6c
	ds_read_b128 v[70:73], v70
	v_lshl_or_b32 v101, v88, 4, v104
	s_waitcnt lgkmcnt(7)
	v_mfma_f32_16x16x32_f16 a[4:7], v[58:61], v[92:95], a[4:7]
	v_bitop3_b32 v92, v106, v113, 7 bitop3:0x6c
	ds_read_b128 v[88:91], v101
	s_waitcnt lgkmcnt(7)
	v_mfma_f32_16x16x32_f16 a[8:11], v[58:61], v[96:99], a[8:11]
	v_lshl_or_b32 v96, v92, 4, v107
	ds_read_b128 v[92:95], v96
	s_waitcnt lgkmcnt(7)
	v_mfma_f32_16x16x32_f16 a[12:15], v[58:61], v[66:69], a[12:15]
	ds_read_b128 v[58:61], v114 offset:7168
	s_waitcnt lgkmcnt(7)
	v_mfma_f32_16x16x32_f16 a[0:3], v[54:57], v[76:79], a[0:3]
	ds_read_b128 v[66:69], v109
	s_waitcnt lgkmcnt(7)
	v_mfma_f32_16x16x32_f16 a[4:7], v[54:57], v[80:83], a[4:7]
	ds_read_b128 v[76:79], v110
	s_waitcnt lgkmcnt(7)
	v_mfma_f32_16x16x32_f16 a[8:11], v[54:57], v[84:87], a[8:11]
	ds_read_b128 v[80:83], v111
	s_waitcnt lgkmcnt(7)
	v_mfma_f32_16x16x32_f16 a[12:15], v[54:57], v[62:65], a[12:15]
	ds_read_b128 v[54:57], v108 offset:9216
	s_waitcnt lgkmcnt(7)
	v_mfma_f32_16x16x32_f16 a[0:3], v[50:53], v[70:73], a[0:3]
	ds_read_b128 v[62:65], v115
	s_waitcnt lgkmcnt(7)
	v_mfma_f32_16x16x32_f16 a[4:7], v[50:53], v[88:91], a[4:7]
	ds_read_b128 v[70:73], v116
	s_waitcnt lgkmcnt(7)
	v_mfma_f32_16x16x32_f16 a[8:11], v[50:53], v[92:95], a[8:11]
	ds_read_b128 v[84:87], v117
	s_waitcnt lgkmcnt(7)
	v_mfma_f32_16x16x32_f16 a[12:15], v[50:53], v[58:61], a[12:15]
	ds_read_b128 v[50:53], v114 offset:9216
	s_waitcnt lgkmcnt(7)
	v_mfma_f32_16x16x32_f16 a[0:3], v[46:49], v[66:69], a[0:3]
	ds_read_b128 v[58:61], v122
	s_waitcnt lgkmcnt(7)
	v_mfma_f32_16x16x32_f16 a[4:7], v[46:49], v[76:79], a[4:7]
	ds_read_b128 v[66:69], v125
	s_waitcnt lgkmcnt(7)
	v_mfma_f32_16x16x32_f16 a[8:11], v[46:49], v[80:83], a[8:11]
	v_add_u32_e32 v80, 0x49, v74
	ds_read_b128 v[76:79], v128
	v_lshlrev_b32_e32 v81, 7, v80
	s_waitcnt lgkmcnt(7)
	v_mfma_f32_16x16x32_f16 a[12:15], v[46:49], v[54:57], a[12:15]
	v_bitop3_b32 v46, v80, v75, 7 bitop3:0x6c
	v_lshl_or_b32 v82, v46, 4, v81
	ds_read_b128 v[46:49], v82
	s_waitcnt lgkmcnt(7)
	v_mfma_f32_16x16x32_f16 a[0:3], v[42:45], v[62:65], a[0:3]
	ds_read_b128 v[54:57], v118
	s_waitcnt lgkmcnt(7)
	v_mfma_f32_16x16x32_f16 a[4:7], v[42:45], v[70:73], a[4:7]
	ds_read_b128 v[62:65], v119
	s_waitcnt lgkmcnt(7)
	v_mfma_f32_16x16x32_f16 a[8:11], v[42:45], v[84:87], a[8:11]
	ds_read_b128 v[70:73], v100
	s_waitcnt lgkmcnt(7)
	v_mfma_f32_16x16x32_f16 a[12:15], v[42:45], v[50:53], a[12:15]
	v_bitop3_b32 v42, v80, v113, 7 bitop3:0x6c
	v_lshl_or_b32 v80, v42, 4, v81
	ds_read_b128 v[42:45], v80
	s_waitcnt lgkmcnt(7)
	v_mfma_f32_16x16x32_f16 a[0:3], v[38:41], v[58:61], a[0:3]
	ds_read_b128 v[50:53], v105
	s_waitcnt lgkmcnt(7)
	v_mfma_f32_16x16x32_f16 a[4:7], v[38:41], v[66:69], a[4:7]
	ds_read_b128 v[58:61], v120
	s_waitcnt lgkmcnt(7)
	v_mfma_f32_16x16x32_f16 a[8:11], v[38:41], v[76:79], a[8:11]
	v_add_u32_e32 v76, 0x4a, v74
	ds_read_b128 v[66:69], v108 offset:7168
	v_lshlrev_b32_e32 v77, 7, v76
	s_waitcnt lgkmcnt(7)
	v_mfma_f32_16x16x32_f16 a[12:15], v[38:41], v[46:49], a[12:15]
	v_bitop3_b32 v38, v76, v75, 7 bitop3:0x6c
	v_lshl_or_b32 v78, v38, 4, v77
	ds_read_b128 v[38:41], v78
	s_waitcnt lgkmcnt(7)
	v_mfma_f32_16x16x32_f16 a[0:3], v[34:37], v[54:57], a[0:3]
	ds_read_b128 v[46:49], v101
	s_waitcnt lgkmcnt(7)
	v_mfma_f32_16x16x32_f16 a[4:7], v[34:37], v[62:65], a[4:7]
	ds_read_b128 v[54:57], v96
	s_waitcnt lgkmcnt(7)
	v_mfma_f32_16x16x32_f16 a[8:11], v[34:37], v[70:73], a[8:11]
	ds_read_b128 v[62:65], v114 offset:7168
	s_waitcnt lgkmcnt(7)
	v_mfma_f32_16x16x32_f16 a[12:15], v[34:37], v[42:45], a[12:15]
	v_bitop3_b32 v34, v76, v113, 7 bitop3:0x6c
	v_lshl_or_b32 v70, v34, 4, v77
	ds_read_b128 v[34:37], v70
	s_waitcnt lgkmcnt(7)
	v_mfma_f32_16x16x32_f16 a[0:3], v[30:33], v[50:53], a[0:3]
	ds_read_b128 v[42:45], v110
	s_waitcnt lgkmcnt(7)
	v_mfma_f32_16x16x32_f16 a[4:7], v[30:33], v[58:61], a[4:7]
	ds_read_b128 v[50:53], v111
	s_waitcnt lgkmcnt(7)
	v_mfma_f32_16x16x32_f16 a[8:11], v[30:33], v[66:69], a[8:11]
	v_add_u32_e32 v66, 0x5a, v74
	ds_read_b128 v[58:61], v108 offset:9216
	v_lshlrev_b32_e32 v67, 7, v66
	s_waitcnt lgkmcnt(7)
	v_mfma_f32_16x16x32_f16 a[12:15], v[30:33], v[38:41], a[12:15]
	v_bitop3_b32 v30, v66, v75, 7 bitop3:0x6c
	v_lshl_or_b32 v30, v30, 4, v67
	ds_read_b128 v[30:33], v30
	s_waitcnt lgkmcnt(7)
	v_mfma_f32_16x16x32_f16 a[0:3], v[26:29], v[46:49], a[0:3]
	ds_read_b128 v[38:41], v116
	s_waitcnt lgkmcnt(7)
	v_mfma_f32_16x16x32_f16 a[4:7], v[26:29], v[54:57], a[4:7]
	ds_read_b128 v[46:49], v117
	s_waitcnt lgkmcnt(7)
	v_mfma_f32_16x16x32_f16 a[8:11], v[26:29], v[62:65], a[8:11]
	ds_read_b128 v[54:57], v114 offset:9216
	s_waitcnt lgkmcnt(7)
	v_mfma_f32_16x16x32_f16 a[12:15], v[26:29], v[34:37], a[12:15]
	v_bitop3_b32 v26, v66, v113, 7 bitop3:0x6c
	v_lshl_or_b32 v26, v26, 4, v67
	ds_read_b128 v[26:29], v26
	s_waitcnt lgkmcnt(7)
	v_mfma_f32_16x16x32_f16 a[0:3], v[22:25], v[42:45], a[0:3]
	ds_read_b128 v[34:37], v125
	s_waitcnt lgkmcnt(7)
	v_mfma_f32_16x16x32_f16 a[4:7], v[22:25], v[50:53], a[4:7]
	ds_read_b128 v[42:45], v128
	s_waitcnt lgkmcnt(7)
	v_mfma_f32_16x16x32_f16 a[8:11], v[22:25], v[58:61], a[8:11]
	v_add_u32_e32 v58, 0x5b, v74
	ds_read_b128 v[50:53], v82
	v_lshlrev_b32_e32 v59, 7, v58
	s_waitcnt lgkmcnt(7)
	v_mfma_f32_16x16x32_f16 a[12:15], v[22:25], v[30:33], a[12:15]
	v_bitop3_b32 v22, v58, v75, 7 bitop3:0x6c
	v_lshl_or_b32 v22, v22, 4, v59
	ds_read_b128 v[22:25], v22
	s_waitcnt lgkmcnt(7)
	v_mfma_f32_16x16x32_f16 a[0:3], v[18:21], v[38:41], a[0:3]
	ds_read_b128 v[30:33], v119
	s_waitcnt lgkmcnt(7)
	v_mfma_f32_16x16x32_f16 a[4:7], v[18:21], v[46:49], a[4:7]
	ds_read_b128 v[38:41], v100
	s_waitcnt lgkmcnt(7)
	v_mfma_f32_16x16x32_f16 a[8:11], v[18:21], v[54:57], a[8:11]
	ds_read_b128 v[46:49], v80
	s_waitcnt lgkmcnt(7)
	v_mfma_f32_16x16x32_f16 a[12:15], v[18:21], v[26:29], a[12:15]
	v_bitop3_b32 v18, v58, v113, 7 bitop3:0x6c
	v_lshl_or_b32 v18, v18, 4, v59
	ds_read_b128 v[18:21], v18
	s_waitcnt lgkmcnt(7)
	v_mfma_f32_16x16x32_f16 a[0:3], v[14:17], v[34:37], a[0:3]
	ds_read_b128 v[26:29], v120
	s_waitcnt lgkmcnt(7)
	v_mfma_f32_16x16x32_f16 a[4:7], v[14:17], v[42:45], a[4:7]
	ds_read_b128 v[34:37], v108 offset:7168
	s_waitcnt lgkmcnt(7)
	v_mfma_f32_16x16x32_f16 a[8:11], v[14:17], v[50:53], a[8:11]
	v_add_u32_e32 v50, 0x5c, v74
	ds_read_b128 v[42:45], v78
	v_lshlrev_b32_e32 v51, 7, v50
	s_waitcnt lgkmcnt(7)
	v_mfma_f32_16x16x32_f16 a[12:15], v[14:17], v[22:25], a[12:15]
	v_bitop3_b32 v14, v50, v75, 7 bitop3:0x6c
	v_lshl_or_b32 v14, v14, 4, v51
	ds_read_b128 v[14:17], v14
	s_waitcnt lgkmcnt(7)
	v_mfma_f32_16x16x32_f16 a[0:3], v[10:13], v[30:33], a[0:3]
	ds_read_b128 v[22:25], v96
	s_waitcnt lgkmcnt(7)
	v_mfma_f32_16x16x32_f16 a[4:7], v[10:13], v[38:41], a[4:7]
	ds_read_b128 v[30:33], v114 offset:7168
	s_waitcnt lgkmcnt(7)
	v_mfma_f32_16x16x32_f16 a[8:11], v[10:13], v[46:49], a[8:11]
	ds_read_b128 v[38:41], v70
	s_waitcnt lgkmcnt(7)
	v_mfma_f32_16x16x32_f16 a[12:15], v[10:13], v[18:21], a[12:15]
	v_bitop3_b32 v10, v50, v113, 7 bitop3:0x6c
	v_lshl_or_b32 v10, v10, 4, v51
	ds_read_b128 v[10:13], v10
	s_waitcnt lgkmcnt(7)
	v_mfma_f32_16x16x32_f16 a[0:3], v[6:9], v[26:29], a[0:3]
	v_lshl_or_b32 v26, s15, 7, v74
	s_waitcnt lgkmcnt(6)
	v_mfma_f32_16x16x32_f16 a[4:7], v[6:9], v[34:37], a[4:7]
	s_waitcnt lgkmcnt(5)
	v_mfma_f32_16x16x32_f16 a[8:11], v[6:9], v[42:45], a[8:11]
	s_waitcnt lgkmcnt(4)
	v_mfma_f32_16x16x32_f16 a[12:15], v[6:9], v[14:17], a[12:15]
	s_waitcnt lgkmcnt(3)
	v_mfma_f32_16x16x32_f16 a[0:3], v[2:5], v[22:25], a[0:3]
	s_nop 7
	v_accvgpr_read_b32 v6, a0
	v_accvgpr_read_b32 v20, a1
	v_accvgpr_read_b32 v21, a2
	v_accvgpr_read_b32 v7, a3
	s_waitcnt lgkmcnt(2)
	v_mfma_f32_16x16x32_f16 a[0:3], v[2:5], v[30:33], a[4:7]
	v_mul_f32_e32 v24, v20, v20
	v_fmac_f32_e32 v24, v6, v6
	v_fmac_f32_e32 v24, v21, v21
	s_nop 4
	v_accvgpr_read_b32 v14, a2
	v_accvgpr_read_b32 v15, a3
	s_waitcnt lgkmcnt(1)
	v_mfma_f32_16x16x32_f16 a[2:5], v[2:5], v[38:41], a[8:11]
	v_accvgpr_read_b32 v8, a0
	v_accvgpr_read_b32 v9, a1
	s_nop 5
	v_accvgpr_read_b32 v18, a4
	v_accvgpr_read_b32 v19, a5
	s_waitcnt lgkmcnt(0)
	v_mfma_f32_16x16x32_f16 a[4:7], v[2:5], v[10:13], a[12:15]
	v_lshlrev_b32_e32 v2, 5, v112
	v_mov_b32_e32 v3, 0
	v_lshl_add_u64 v[12:13], s[6:7], 0, v[2:3]
	v_lshlrev_b32_e32 v2, 3, v75
	v_lshl_add_u64 v[12:13], v[12:13], 0, v[2:3]
	v_add_f32_e32 v2, 0, v6
	v_add_f32_e32 v2, v2, v20
	v_add_f32_e32 v2, v2, v21
	v_add_f32_e32 v25, v2, v7
	v_or_b32_e32 v2, s14, v26
	v_lshlrev_b64 v[22:23], 7, v[2:3]
	v_cvt_pk_f16_f32 v21, v21, v7
	v_cvt_pk_f16_f32 v20, v6, v20
	v_lshl_add_u64 v[22:23], v[12:13], 0, v[22:23]
	v_pk_mov_b32 v[6:7], v[6:7], v[8:9] op_sel:[1,0]
	global_store_dwordx2 v[22:23], v[20:21], off
	v_accvgpr_read_b32 v21, a1
	v_pk_mul_f32 v[6:7], v[6:7], v[6:7]
	v_add_f32_e32 v2, v25, v8
	v_accvgpr_read_b32 v20, a0
	v_add_f32_e32 v6, v24, v6
	v_add_f32_e32 v22, v6, v7
	v_add_f32_e32 v2, v2, v9
	v_pk_mul_f32 v[6:7], v[14:15], v[14:15]
	v_pk_mul_f32 v[20:21], v[20:21], v[20:21]
	v_add_f32_e32 v2, v2, v14
	v_add_f32_e32 v7, v22, v21
	v_add_u32_e32 v22, s14, v26
	v_add_f32_e32 v21, v2, v15
	v_add_u32_e32 v2, 0x80, v22
	v_add_f32_e32 v20, v7, v6
	v_cvt_pk_f16_f32 v6, v8, v9
	v_lshlrev_b64 v[8:9], 7, v[2:3]
	v_accvgpr_read_b32 v16, a2
	v_accvgpr_read_b32 v17, a3
	v_cvt_pk_f16_f32 v7, v14, v15
	v_lshl_add_u64 v[8:9], v[12:13], 0, v[8:9]
	global_store_dwordx2 v[8:9], v[6:7], off
	v_add_f32_e32 v2, v21, v16
	v_pk_mov_b32 v[6:7], v[14:15], v[16:17] op_sel:[1,0]
	v_accvgpr_read_b32 v9, a3
	v_pk_mul_f32 v[6:7], v[6:7], v[6:7]
	v_add_f32_e32 v2, v2, v17
	v_accvgpr_read_b32 v8, a2
	v_add_f32_e32 v6, v20, v6
	v_add_f32_e32 v2, v2, v18
	v_add_f32_e32 v14, v6, v7
	v_pk_mul_f32 v[6:7], v[18:19], v[18:19]
	v_pk_mul_f32 v[8:9], v[8:9], v[8:9]
	v_add_f32_e32 v15, v2, v19
	v_add_u32_e32 v2, 0x100, v22
	v_add_f32_e32 v7, v14, v9
	v_lshlrev_b64 v[8:9], 7, v[2:3]
	v_accvgpr_read_b32 v4, a4
	v_accvgpr_read_b32 v5, a5
	v_add_f32_e32 v14, v7, v6
	v_cvt_pk_f16_f32 v7, v18, v19
	v_cvt_pk_f16_f32 v6, v16, v17
	v_lshl_add_u64 v[8:9], v[12:13], 0, v[8:9]
	global_store_dwordx2 v[8:9], v[6:7], off
	v_pk_mov_b32 v[6:7], v[18:19], v[4:5] op_sel:[1,0]
	v_accvgpr_read_b32 v9, a5
	v_pk_mul_f32 v[6:7], v[6:7], v[6:7]
	v_add_f32_e32 v2, v15, v4
	v_accvgpr_read_b32 v8, a4
	v_add_f32_e32 v6, v14, v6
	v_accvgpr_read_b32 v10, a6
	v_accvgpr_read_b32 v11, a7
	v_add_f32_e32 v7, v6, v7
	v_add_f32_e32 v2, v2, v5
	v_pk_mul_f32 v[8:9], v[8:9], v[8:9]
	v_add_f32_e32 v6, v2, v10
	v_pk_mul_f32 v[14:15], v[10:11], v[10:11]
	v_add_f32_e32 v2, v7, v9
	v_add_f32_e32 v9, v2, v14
	v_or_b32_e32 v2, s3, v74
	v_or_b32_e32 v2, s14, v2
	v_cvt_pk_f16_f32 v14, v4, v5
	v_lshlrev_b64 v[4:5], 7, v[2:3]
	v_mul_f32_e32 v7, v11, v11
	v_cvt_pk_f16_f32 v15, v10, v11
	v_lshl_add_u64 v[4:5], v[12:13], 0, v[4:5]
	v_accvgpr_read_b32 v8, a7
	global_store_dwordx2 v[4:5], v[14:15], off
	v_pk_add_f32 v[4:5], v[6:7], v[8:9]
	v_mov_b32_e32 v2, v3
	s_nop 0
	v_mov_b32_dpp v6, v4 row_shr:1 row_mask:0xf bank_mask:0xf bound_ctrl:1
	v_mov_b32_dpp v7, v5 row_shr:1 row_mask:0xf bank_mask:0xf bound_ctrl:1
	v_pk_add_f32 v[4:5], v[4:5], v[6:7]
	s_nop 1
	v_mov_b32_dpp v6, v4 row_shr:2 row_mask:0xf bank_mask:0xf bound_ctrl:1
	v_mov_b32_dpp v7, v5 row_shr:2 row_mask:0xf bank_mask:0xf bound_ctrl:1
	v_pk_add_f32 v[4:5], v[4:5], v[6:7]
	s_nop 1
	v_mov_b32_dpp v6, v4 row_shr:4 row_mask:0xf bank_mask:0xf bound_ctrl:1
	v_mov_b32_dpp v7, v5 row_shr:4 row_mask:0xf bank_mask:0xf bound_ctrl:1
	v_pk_add_f32 v[4:5], v[4:5], v[6:7]
	s_nop 1
	v_mov_b32_dpp v6, v4 row_shr:8 row_mask:0xf bank_mask:0xf bound_ctrl:1
	v_mov_b32_dpp v7, v5 row_shr:8 row_mask:0xf bank_mask:0xf bound_ctrl:1
	v_pk_add_f32 v[4:5], v[4:5], v[6:7]
	v_mov_b32_e32 v6, v3
	v_mov_b32_e32 v7, v3
	s_nop 0
	v_mov_b32_dpp v6, v4 row_bcast:15 row_mask:0xa bank_mask:0xf
	v_mov_b32_dpp v7, v5 row_bcast:15 row_mask:0xa bank_mask:0xf
	v_pk_add_f32 v[4:5], v[4:5], v[6:7]
	s_nop 1
	v_mov_b32_dpp v2, v4 row_bcast:31 row_mask:0xc bank_mask:0xf
	v_mov_b32_dpp v3, v5 row_bcast:31 row_mask:0xc bank_mask:0xf
	s_and_saveexec_b64 s[6:7], s[4:5]
	v_pk_add_f32 v[2:3], v[4:5], v[2:3]
	ds_write_b64 v1, v[2:3] offset:14080
	s_or_b64 exec, exec, s[6:7]
	v_cmp_eq_u32_e32 vcc, 0, v0
	s_waitcnt lgkmcnt(0)
	s_barrier
	s_and_saveexec_b64 s[4:5], vcc
	s_cbranch_execz .LBB1_14
	v_mov_b32_e32 v8, 0
	ds_read_b128 v[0:3], v8 offset:14080
	ds_read_b128 v[4:7], v8 offset:14096
	s_lshl_b32 s2, s2, 1
	s_mov_b32 s3, 0
	s_lshl_b64 s[2:3], s[2:3], 2
	s_waitcnt lgkmcnt(0)
	v_pk_add_f32 v[0:1], v[0:1], v[2:3]
	s_add_u32 s0, s22, s2
	v_pk_add_f32 v[0:1], v[0:1], v[4:5]
	s_addc_u32 s1, s23, s3
	v_pk_add_f32 v[0:1], v[0:1], v[6:7]
	global_store_dwordx2 v8, v[0:1], s[0:1]

	.amdhsa_kernel _Z4khidPKDF16_PKfS2_S2_S0_PDF16_Pf
		.amdhsa_group_segment_fixed_size 14112
		.amdhsa_private_segment_fixed_size 0
		.amdhsa_kernarg_size 56
		.amdhsa_user_sgpr_count 2
		.amdhsa_user_sgpr_dispatch_ptr 0
		.amdhsa_user_sgpr_queue_ptr 0
		.amdhsa_user_sgpr_kernarg_segment_ptr 1
		.amdhsa_user_sgpr_dispatch_id 0
		.amdhsa_user_sgpr_kernarg_preload_length 0
		.amdhsa_user_sgpr_kernarg_preload_offset 0
		.amdhsa_user_sgpr_private_segment_size 0
		.amdhsa_uses_dynamic_stack 0
		.amdhsa_enable_private_segment 0
		.amdhsa_system_sgpr_workgroup_id_x 1
		.amdhsa_system_sgpr_workgroup_id_y 0
		.amdhsa_system_sgpr_workgroup_id_z 0
		.amdhsa_system_sgpr_workgroup_info 0
		.amdhsa_system_vgpr_workitem_id 0
		.amdhsa_next_free_vgpr 156
		.amdhsa_next_free_sgpr 24
		.amdhsa_accum_offset 140
		.amdhsa_reserve_vcc 1
		.amdhsa_float_round_mode_32 0
		.amdhsa_float_round_mode_16_64 0
		.amdhsa_float_denorm_mode_32 3
		.amdhsa_float_denorm_mode_16_64 3
		.amdhsa_dx10_clamp 1
		.amdhsa_ieee_mode 1
		.amdhsa_fp16_overflow 0
		.amdhsa_tg_split 0
		.amdhsa_exception_fp_ieee_invalid_op 0
		.amdhsa_exception_fp_denorm_src 0
		.amdhsa_exception_fp_ieee_div_zero 0
		.amdhsa_exception_fp_ieee_overflow 0
		.amdhsa_exception_fp_ieee_underflow 0
		.amdhsa_exception_fp_ieee_inexact 0
		.amdhsa_exception_int_div_zero 0
	.end_amdhsa_kernel

amdhsa.kernels:
  - .agpr_count:     0
    .args:
      - .actual_access:  read_only
        .address_space:  global
        .offset:         0
        .size:           8
        .value_kind:     global_buffer
      - .actual_access:  read_only
        .address_space:  global
        .offset:         8
        .size:           8
        .value_kind:     global_buffer
      - .actual_access:  read_only
        .address_space:  global
        .offset:         16
        .size:           8
        .value_kind:     global_buffer
      - .actual_access:  read_only
        .address_space:  global
        .offset:         24
        .size:           8
        .value_kind:     global_buffer
      - .actual_access:  read_only
        .address_space:  global
        .offset:         32
        .size:           8
        .value_kind:     global_buffer
      - .actual_access:  read_only
        .address_space:  global
        .offset:         40
        .size:           8
        .value_kind:     global_buffer
      - .actual_access:  write_only
        .address_space:  global
        .offset:         48
        .size:           8
        .value_kind:     global_buffer
      - .actual_access:  write_only
        .address_space:  global
        .offset:         56
        .size:           8
        .value_kind:     global_buffer
      - .actual_access:  write_only
        .address_space:  global
        .offset:         64
        .size:           8
        .value_kind:     global_buffer
      - .actual_access:  write_only
        .address_space:  global
        .offset:         72
        .size:           8
        .value_kind:     global_buffer
    .group_segment_fixed_size: 12000
    .kernarg_segment_align: 8
    .kernarg_segment_size: 80
    .language:       OpenCL C
    .language_version:
      - 2
      - 0
    .max_flat_workgroup_size: 256
    .name:           _Z2k0PKfS0_S0_S0_S0_S0_PDF16_PfS1_S1_
    .private_segment_fixed_size: 0
    .sgpr_count:     24
    .sgpr_spill_count: 0
    .symbol:         _Z2k0PKfS0_S0_S0_S0_S0_PDF16_PfS1_S1_.kd
    .uniform_work_group_size: 1
    .uses_dynamic_stack: false
    .vgpr_count:     150
    .vgpr_spill_count: 0
    .wavefront_size: 64
  - .agpr_count:     16
    .args:
      - .actual_access:  read_only
        .address_space:  global
        .offset:         0
        .size:           8
        .value_kind:     global_buffer
      - .actual_access:  read_only
        .address_space:  global
        .offset:         8
        .size:           8
        .value_kind:     global_buffer
      - .actual_access:  read_only
        .address_space:  global
        .offset:         16
        .size:           8
        .value_kind:     global_buffer
      - .actual_access:  read_only
        .address_space:  global
        .offset:         24
        .size:           8
        .value_kind:     global_buffer
      - .actual_access:  read_only
        .address_space:  global
        .offset:         32
        .size:           8
        .value_kind:     global_buffer
      - .actual_access:  write_only
        .address_space:  global
        .offset:         40
        .size:           8
        .value_kind:     global_buffer
      - .actual_access:  write_only
        .address_space:  global
        .offset:         48
        .size:           8
        .value_kind:     global_buffer
    .group_segment_fixed_size: 14112
    .kernarg_segment_align: 8
    .kernarg_segment_size: 56
    .language:       OpenCL C
    .language_version:
      - 2
      - 0
    .max_flat_workgroup_size: 256
    .name:           _Z4khidPKDF16_PKfS2_S2_S0_PDF16_Pf
    .private_segment_fixed_size: 0
    .sgpr_count:     30
    .sgpr_spill_count: 0
    .symbol:         _Z4khidPKDF16_PKfS2_S2_S0_PDF16_Pf.kd
    .uniform_work_group_size: 1
    .uses_dynamic_stack: false
    .vgpr_count:     156
    .vgpr_spill_count: 0
    .wavefront_size: 64
  - .agpr_count:     144
    .args:
      - .actual_access:  read_only
        .address_space:  global
        .offset:         0
        .size:           8
        .value_kind:     global_buffer
      - .actual_access:  read_only
        .address_space:  global
        .offset:         8
        .size:           8
        .value_kind:     global_buffer
      - .actual_access:  read_only
        .address_space:  global
        .offset:         16
        .size:           8
        .value_kind:     global_buffer
      - .actual_access:  read_only
        .address_space:  global
        .offset:         24
        .size:           8
        .value_kind:     global_buffer
      - .address_space:  global
        .offset:         32
        .size:           8
        .value_kind:     global_buffer
      - .address_space:  global
        .offset:         40
        .size:           8
        .value_kind:     global_buffer
      - .address_space:  global
        .offset:         48
        .size:           8
        .value_kind:     global_buffer
    .group_segment_fixed_size: 0
    .kernarg_segment_align: 8
    .kernarg_segment_size: 56
    .language:       OpenCL C
    .language_version:
      - 2
      - 0
    .max_flat_workgroup_size: 256
    .name:           _Z6kfinalPKDF16_PKfS2_S2_PK15HIP_vector_typeIjLj4EES2_Pf
    .private_segment_fixed_size: 0
    .sgpr_count:     41
    .sgpr_spill_count: 0
    .symbol:         _Z6kfinalPKDF16_PKfS2_S2_PK15HIP_vector_typeIjLj4EES2_Pf.kd
    .uniform_work_group_size: 1
    .uses_dynamic_stack: false
    .vgpr_count:     400
    .vgpr_spill_count: 0
    .wavefront_size: 64
  - .agpr_count:     73
    .args:
      - .actual_access:  read_only
        .address_space:  global
        .offset:         0
        .size:           8
        .value_kind:     global_buffer
      - .actual_access:  read_only
        .address_space:  global
        .offset:         8
        .size:           8
        .value_kind:     global_buffer
      - .actual_access:  read_only
        .address_space:  global
        .offset:         16
        .size:           8
        .value_kind:     global_buffer
      - .actual_access:  read_only
        .address_space:  global
        .offset:         24
        .size:           8
        .value_kind:     global_buffer
      - .address_space:  global
        .offset:         32
        .size:           8
        .value_kind:     global_buffer
      - .address_space:  global
        .offset:         40
        .size:           8
        .value_kind:     global_buffer
      - .address_space:  global
        .offset:         48
        .size:           8
        .value_kind:     global_buffer
    .group_segment_fixed_size: 0
    .kernarg_segment_align: 8
    .kernarg_segment_size: 56
    .language:       OpenCL C
    .language_version:
      - 2
      - 0
    .max_flat_workgroup_size: 512
    .name:           _Z7kfinal3PKDF16_PKfS2_S2_PK15HIP_vector_typeIjLj4EES2_Pf
    .private_segment_fixed_size: 0
    .sgpr_count:     60
    .sgpr_spill_count: 0
    .symbol:         _Z7kfinal3PKDF16_PKfS2_S2_PK15HIP_vector_typeIjLj4EES2_Pf.kd
    .uniform_work_group_size: 1
    .uses_dynamic_stack: false
    .vgpr_count:     253
    .vgpr_spill_count: 0
    .wavefront_size: 64
